# speedup vs baseline: 1.0102x; 1.0102x over previous
.LBB5_15:
	s_or_b64 exec, exec, s[6:7]
	s_load_dwordx4 s[4:7], s[0:1], 0x18
	v_mov_b32_e32 v17, 0
	s_waitcnt lgkmcnt(0)
	s_barrier
	ds_read_b32 v17, v17 offset:32776
	s_and_b32 s17, s5, 0xffff
	s_and_b32 s21, s15, 0xffff
	v_accvgpr_read_b32 v56, a0
	v_lshlrev_b32_e32 v15, 12, v1
	v_lshlrev_b32_e32 v18, 4, v56
	s_add_u32 s8, s4, s7
	s_mov_b32 s16, s4
	v_lshlrev_b32_e32 v14, 14, v10
	v_lshlrev_b32_e32 v16, 7, v0
	s_addc_u32 s9, s5, 0
	s_waitcnt lgkmcnt(0)
	v_cmp_ne_u32_e64 s[4:5], 0, v17
	v_add_u32_e32 v17, 0, v15
	v_or_b32_e32 v15, v18, v15
	v_or3_b32 v15, v16, v14, v15
	v_lshlrev_b32_e32 v13, 3, v0
	v_accvgpr_write_b32 a98, v15
	v_and_b32_e32 v15, 63, v57
	v_lshlrev_b32_e32 v19, 4, v13
	v_lshrrev_b32_e32 v15, 5, v15
	s_waitcnt vmcnt(1)
	v_mul_f32_e32 v45, 0xbfb8aa3b, v6
	v_mul_f32_e32 v6, 0xbfb8aa3b, v7
	v_mul_f32_e32 v7, 0xbfb8aa3b, v9
	v_lshlrev_b32_e32 v9, 8, v1
	v_add3_u32 v17, v17, v19, v18
	v_accvgpr_write_b32 a94, v15
	v_bfe_u32 v16, v57, 2, 3
	v_lshlrev_b32_e32 v15, 3, v57
	v_add_u32_e32 v9, v23, v9
	v_accvgpr_write_b32 a97, v17
	v_and_b32_e32 v17, 24, v15
	v_lshlrev_b32_e32 v10, 13, v10
	v_lshlrev_b32_e32 v15, 10, v16
	v_or_b32_e32 v9, v9, v13
	v_or3_b32 v10, v10, v15, v17
	v_cmp_eq_u32_e64 s[2:3], 3, v1
	v_lshl_add_u32 v9, v9, 1, s6
	v_accvgpr_write_b32 a95, v16
	v_lshl_add_u32 v16, v10, 1, s44
	v_lshlrev_b32_e32 v1, 7, v1
	v_and_b32_e32 v10, 8, v57
	v_lshlrev_b32_e32 v0, 1, v0
	v_or3_b32 v1, v1, v10, v0
	v_add_u32_e32 v10, s24, v9
	s_lshl_b32 s6, s33, 9
	v_or3_b32 v1, v1, v18, v14
	v_accvgpr_write_b32 a99, v10
	v_add_u32_e32 v10, s26, v9
	v_add_u32_e32 v1, s6, v1
	s_and_b32 s33, s6, 0xe00
	s_lshl_b32 s6, s42, 9
	v_accvgpr_write_b32 a102, v10
	v_add_u32_e32 v10, s28, v9
	s_and_b32 s35, s6, 0xe00
	s_lshl_b32 s6, s43, 9
	v_accvgpr_write_b32 a103, v10
	v_add_u32_e32 v10, s30, v9
	s_and_b32 s37, s6, 0xe00
	s_lshl_b32 s6, s45, 9
	v_accvgpr_write_b32 a104, v10
	v_add_u32_e32 v10, s34, v9
	v_accvgpr_write_b32 a96, v17
	v_ashrrev_i32_e32 v17, 31, v16
	s_and_b32 s39, s6, 0xe00
	s_lshl_b32 s6, s46, 9
	v_accvgpr_write_b32 a105, v10
	v_add_u32_e32 v10, s36, v9
	v_accvgpr_write_b32 a93, v17
	s_and_b32 s41, s6, 0xe00
	s_lshl_b32 s6, s47, 9
	v_accvgpr_write_b32 a106, v10
	v_add_u32_e32 v10, s38, v9
	v_add_u32_e32 v9, s40, v9
	v_or_b32_e32 v13, v13, v56
	v_accvgpr_write_b32 a92, v16
	v_lshl_add_u64 v[16:17], s[8:9], 0, v[16:17]
	s_and_b32 s42, s6, 0xe00
	s_lshl_b32 s6, s48, 9
	v_accvgpr_write_b32 a108, v9
	v_lshlrev_b32_e32 v9, 1, v12
	s_mov_b32 s19, 0x20000
	v_accvgpr_write_b32 a101, v17
	s_and_b32 s43, s6, 0xe00
	s_lshl_b32 s6, s49, 9
	v_accvgpr_write_b32 a107, v10
	v_add3_u32 v0, 0, v9, v0
	v_lshlrev_b32_e32 v9, 9, v11
	v_lshlrev_b32_e32 v10, 4, v13
	s_brev_b32 s18, -2
	s_mov_b32 s22, 0x80000
	s_mov_b32 s23, s19
	s_mov_b32 s20, s14
	v_cmp_gt_u32_e64 s[0:1], 8, v22
	s_mov_b32 s15, 0
	v_accvgpr_write_b32 a100, v16
	s_and_b32 s44, s6, 0xe00
	v_add3_u32 v9, 0, v9, v10
	s_mov_b64 s[26:27], 0
	s_mov_b32 s34, 0x80008000
	s_mov_b32 s36, 0x100000
	s_brev_b32 s38, 60
	s_mov_b32 s40, 0xbc38aa3b
	s_mov_b32 s45, 0x41000000
	s_waitcnt vmcnt(0)
	v_accvgpr_write_b32 a112, v250
	v_accvgpr_write_b32 a113, v251
	v_accvgpr_write_b32 a114, v252
	v_accvgpr_write_b32 a115, v253
	v_accvgpr_write_b32 a116, v2
	v_accvgpr_write_b32 a117, v3
	v_accvgpr_write_b32 a118, v4
	v_accvgpr_write_b32 a119, v5
	v_and_b32_e32 v46, 2, v57
	v_cmp_ne_u32_e64 s[0:1], 0, v46
	v_and_b32_e32 v46, 32, v57
	v_cmp_ne_u32_e64 s[30:31], 0, v46
	v_mov_b32_e32 v26, 0x44444444
	v_mov_b32_e32 v46, 0xeeeeeeee
	v_cndmask_b32_e64 v26, v26, v46, s[0:1]
	v_accvgpr_read_b32 v46, a98
	v_bfe_u32 v47, v57, 4, 2
	v_lshlrev_b32_e32 v47, 7, v47
	v_sub_u32_e32 v46, v46, v47
	v_and_b32_e32 v47, 7, v57
	v_lshlrev_b32_e32 v47, 4, v47
	v_sub_u32_e32 v46, v46, v47
	v_bfe_u32 v47, v57, 4, 1
	v_lshl_add_u32 v46, v47, 8, v46
	v_and_b32_e32 v47, 15, v57
	v_lshl_add_u32 v46, v47, 4, v46
	v_mov_b32_e32 v47, s33
	v_mov_b32_e32 v48, s35
	v_cndmask_b32_e64 v47, v47, v48, s[30:31]
	v_or_b32_e32 v27, v46, v47
	v_mov_b32_e32 v47, s37
	v_mov_b32_e32 v48, s39
	v_cndmask_b32_e64 v47, v47, v48, s[30:31]
	v_or_b32_e32 v28, v46, v47
	v_mov_b32_e32 v47, s41
	v_mov_b32_e32 v48, s42
	v_cndmask_b32_e64 v47, v47, v48, s[30:31]
	v_or_b32_e32 v29, v46, v47
	v_mov_b32_e32 v47, s43
	v_mov_b32_e32 v48, s44
	v_cndmask_b32_e64 v47, v47, v48, s[30:31]
	v_or_b32_e32 v30, v46, v47
	v_lshrrev_b32_e32 v46, 6, v57
	v_lshlrev_b32_e32 v46, 7, v46
	v_and_b32_e32 v47, 8, v57
	v_bfe_u32 v48, v57, 4, 2
	v_lshl_or_b32 v47, v48, 1, v47
	v_add_u32_e32 v46, v46, v47
	v_and_b32_e32 v47, 7, v57
	v_lshl_add_u32 v46, v47, 4, v46
	v_sub_u32_e32 v1, v1, v46
	v_bfe_u32 v46, v57, 7, 1
	v_lshlrev_b32_e32 v46, 8, v46
	v_bfe_u32 v47, v57, 1, 2
	v_lshl_or_b32 v46, v47, 6, v46
	v_bfe_u32 v47, v57, 5, 1
	v_lshl_or_b32 v46, v47, 5, v46
	v_and_b32_e32 v47, 1, v57
	v_lshl_or_b32 v46, v47, 4, v46
	v_bfe_u32 v47, v57, 3, 1
	v_bfe_u32 v48, v57, 6, 1
	v_lshl_or_b32 v47, v48, 1, v47
	v_lshl_or_b32 v46, v47, 2, v46
	v_bfe_u32 v47, v57, 4, 1
	v_lshl_or_b32 v46, v47, 1, v46
	v_add_u32_e32 v1, v1, v46
	v_lshrrev_b32_e32 v46, 6, v57
	v_lshlrev_b32_e32 v46, 12, v46
	v_bfe_u32 v47, v57, 4, 2
	v_lshl_or_b32 v46, v47, 10, v46
	v_and_b32_e32 v47, 3, v57
	v_lshl_or_b32 v46, v47, 2, v46
	v_bfe_u32 v47, v57, 3, 1
	v_bfe_u32 v48, v57, 4, 1
	v_xor_b32_e32 v47, v47, v48
	v_lshl_or_b32 v46, v47, 5, v46
	v_bfe_u32 v47, v57, 5, 1
	v_lshl_or_b32 v46, v47, 7, v46
	v_bfe_u32 v47, v57, 2, 1
	v_lshl_or_b32 v31, v47, 4, v46
	v_xor_b32_e32 v32, 0x80, v31
	v_xor_b32_e32 v47, 1, v47
	v_lshl_or_b32 v33, v47, 4, v46
	v_add_u32_e32 v33, 0x200, v33
	v_xor_b32_e32 v34, 0x80, v33
	v_lshrrev_b32_e32 v46, 3, v57
	v_and_b32_e32 v46, 24, v46
	v_lshrrev_b32_e32 v47, 1, v57
	v_and_or_b32 v46, v47, 4, v46
	v_bfe_u32 v47, v57, 4, 2
	v_or_b32_e32 v46, v46, v47
	v_and_b32_e32 v47, 3, v57
	v_and_b32_e32 v48, 4, v57
	v_lshl_or_b32 v47, v48, 1, v47
	v_xor_b32_e32 v46, v46, v47
	v_and_b32_e32 v47, 7, v57
	v_lshlrev_b32_e32 v47, 9, v47
	v_lshl_or_b32 v9, v46, 4, v47
	v_accvgpr_write_b32 a120, v226
	v_accvgpr_write_b32 a121, v227
	v_accvgpr_write_b32 a122, v228
	v_accvgpr_write_b32 a123, v229
	v_accvgpr_write_b32 a124, v230
	v_accvgpr_write_b32 a125, v231
	v_accvgpr_write_b32 a126, v232
	v_accvgpr_write_b32 a127, v233
	v_accvgpr_write_b32 a128, v234
	v_accvgpr_write_b32 a129, v235
	v_accvgpr_write_b32 a130, v236
	v_accvgpr_write_b32 a131, v237
	v_accvgpr_write_b32 a132, v238
	v_accvgpr_write_b32 a133, v239
	v_accvgpr_write_b32 a134, v240
	v_accvgpr_write_b32 a135, v241
	v_accvgpr_write_b32 a136, v242
	v_accvgpr_write_b32 a137, v243
	v_accvgpr_write_b32 a138, v244
	v_accvgpr_write_b32 a139, v245
	v_accvgpr_write_b32 a140, v246
	v_accvgpr_write_b32 a141, v247
	v_accvgpr_write_b32 a142, v248
	v_accvgpr_write_b32 a143, v249
	v_accvgpr_write_b32 a144, v194
	v_accvgpr_write_b32 a145, v195
	v_accvgpr_write_b32 a146, v196
	v_accvgpr_write_b32 a147, v197
	v_accvgpr_write_b32 a148, v198
	v_accvgpr_write_b32 a149, v199
	v_accvgpr_write_b32 a150, v200
	v_accvgpr_write_b32 a151, v201
	v_accvgpr_write_b32 a152, v202
	v_accvgpr_write_b32 a153, v203
	v_accvgpr_write_b32 a154, v204
	v_accvgpr_write_b32 a155, v205
	v_accvgpr_write_b32 a156, v206
	v_accvgpr_write_b32 a157, v207
	v_accvgpr_write_b32 a158, v208
	v_accvgpr_write_b32 a159, v209
	v_accvgpr_write_b32 a160, v210
	v_accvgpr_write_b32 a161, v211
	v_accvgpr_write_b32 a162, v212
	v_accvgpr_write_b32 a163, v213
	v_accvgpr_write_b32 a164, v214
	v_accvgpr_write_b32 a165, v215
	v_accvgpr_write_b32 a166, v216
	v_accvgpr_write_b32 a167, v217
	v_accvgpr_write_b32 a168, v218
	v_accvgpr_write_b32 a169, v219
	v_accvgpr_write_b32 a170, v220
	v_accvgpr_write_b32 a171, v221
	v_accvgpr_write_b32 a172, v222
	v_accvgpr_write_b32 a173, v223
	v_accvgpr_write_b32 a174, v224
	v_accvgpr_write_b32 a175, v225
	s_mov_b64 s[24:25], 0
	s_mov_b32 s46, 0
	s_mov_b32 s30, 0x3c38aa3b
	s_mov_b32 s31, 0xbc000000
	v_mov_b32_e32 v35, 0
	s_mov_b32 s50, 0
	s_mov_b32 s49, 4
	v_bfe_u32 v50, v57, 4, 2
	v_lshlrev_b32_e32 v50, 4, v50
	v_bfe_u32 v51, v57, 4, 1
	v_bfe_u32 v52, v57, 1, 1
	v_lshlrev_b32_e32 v52, 2, v52
	v_lshl_or_b32 v51, v51, 5, v52
	v_sub_u32_e32 v54, v51, v50
	v_bfe_u32 v51, v57, 2, 2
	v_and_b32_e32 v52, 1, v57
	v_lshl_or_b32 v51, v51, 1, v52
	v_and_b32_e32 v52, 7, v57
	v_sub_u32_e32 v51, v51, v52
	v_lshlrev_b32_e32 v51, 11, v51
	v_add_u32_e32 v54, v54, v51
	v_and_b32_e32 v55, 32, v57
	v_cmp_ne_u32_e64 s[28:29], 0, v55
	v_accvgpr_read_b32 v242, a99
	v_accvgpr_read_b32 v55, a102
	v_cndmask_b32_e64 v242, v242, v55, s[28:29]
	v_add_u32_e32 v242, v242, v54
	v_accvgpr_read_b32 v243, a103
	v_accvgpr_read_b32 v55, a104
	v_cndmask_b32_e64 v243, v243, v55, s[28:29]
	v_add_u32_e32 v243, v243, v54
	v_accvgpr_read_b32 v244, a105
	v_accvgpr_read_b32 v55, a106
	v_cndmask_b32_e64 v244, v244, v55, s[28:29]
	v_add_u32_e32 v244, v244, v54
	v_accvgpr_read_b32 v245, a107
	v_accvgpr_read_b32 v55, a108
	v_cndmask_b32_e64 v245, v245, v55, s[28:29]
	v_add_u32_e32 v245, v245, v54
	s_mov_b64 s[26:27], -1
	v_mov_b32_e32 v10, 0
	v_mov_b32_e32 v11, 0
	v_mov_b32_e32 v12, 0
	v_mov_b32_e32 v13, 0
	v_mov_b32_e32 v14, 0
	v_mov_b32_e32 v15, 0
	v_mov_b32_e32 v16, 0
	v_mov_b32_e32 v17, 0
	v_mov_b32_e32 v18, 0
	v_mov_b32_e32 v19, 0
	v_mov_b32_e32 v20, 0
	v_mov_b32_e32 v21, 0
	v_mov_b32_e32 v22, 0
	v_mov_b32_e32 v23, 0
	v_mov_b32_e32 v24, 0
	v_mov_b32_e32 v25, 0
	v_mov_b32_e32 v2, 0
	v_mov_b32_e32 v3, 0
	v_mov_b32_e32 v4, 0
	v_mov_b32_e32 v5, 0
	v_mov_b32_e32 v250, 0
	v_mov_b32_e32 v251, 0
	v_mov_b32_e32 v252, 0
	v_mov_b32_e32 v253, 0
	v_mov_b32_e32 v46, 0
	v_mov_b32_e32 v47, 0
	v_mov_b32_e32 v48, 0
	v_mov_b32_e32 v49, 0
	v_mov_b32_e32 v50, 0
	v_mov_b32_e32 v51, 0
	v_mov_b32_e32 v52, 0
	v_mov_b32_e32 v53, 0
	buffer_load_dword v226, v242, s[16:19], 0 offen sc1
	buffer_load_dword v227, v242, s[16:19], 0 offen offset:8 sc1
	buffer_load_dword v228, v242, s[16:19], 0 offen offset:16 sc1
	buffer_load_dword v229, v242, s[16:19], 0 offen offset:24 sc1
	buffer_load_dword v230, v243, s[16:19], 0 offen sc1
	buffer_load_dword v231, v243, s[16:19], 0 offen offset:8 sc1
	buffer_load_dword v232, v243, s[16:19], 0 offen offset:16 sc1
	buffer_load_dword v233, v243, s[16:19], 0 offen offset:24 sc1
	buffer_load_dword v234, v244, s[16:19], 0 offen sc1
	buffer_load_dword v235, v244, s[16:19], 0 offen offset:8 sc1
	buffer_load_dword v236, v244, s[16:19], 0 offen offset:16 sc1
	buffer_load_dword v237, v244, s[16:19], 0 offen offset:24 sc1
	buffer_load_dword v238, v245, s[16:19], 0 offen sc1
	buffer_load_dword v239, v245, s[16:19], 0 offen offset:8 sc1
	buffer_load_dword v240, v245, s[16:19], 0 offen offset:16 sc1
	buffer_load_dword v241, v245, s[16:19], 0 offen offset:24 sc1
	s_waitcnt vmcnt(0)

.Lrec_stored:
	s_cmpk_eq_i32 s14, 0x100
	s_cbranch_scc1 .Lrec_exit
	v_and_or_b32 v15, s29, 56, v56
	v_lshl_add_u32 v15, v15, 6, v0
	ds_write_b16 v15, v14 offset:33024
	v_mov_b32_e32 v44, v12
	v_add_u32_e32 v242, s7, v27
	v_add_u32_e32 v243, s7, v28
	v_add_u32_e32 v244, s7, v29
	v_add_u32_e32 v245, s7, v30
	v_xor_b32_e32 v31, 0x4000, v31
	v_xor_b32_e32 v32, 0x4000, v32
	v_xor_b32_e32 v33, 0x4000, v33
	v_xor_b32_e32 v34, 0x4000, v34
	v_xor_b32_e32 v9, 0x4000, v9
	v_mov_b32_e32 v10, 0
	v_mov_b32_e32 v11, 0
	v_mov_b32_e32 v12, 0
	v_mov_b32_e32 v13, 0
	v_mov_b32_e32 v14, 0
	v_mov_b32_e32 v15, 0
	v_mov_b32_e32 v16, 0
	v_mov_b32_e32 v17, 0
	v_mov_b32_e32 v18, 0
	v_mov_b32_e32 v19, 0
	v_mov_b32_e32 v20, 0
	v_mov_b32_e32 v21, 0
	v_mov_b32_e32 v22, 0
	v_mov_b32_e32 v23, 0
	v_mov_b32_e32 v24, 0
	v_mov_b32_e32 v25, 0
	v_mov_b32_e32 v2, 0
	v_mov_b32_e32 v3, 0
	v_mov_b32_e32 v4, 0
	v_mov_b32_e32 v5, 0
	v_mov_b32_e32 v250, 0
	v_mov_b32_e32 v251, 0
	v_mov_b32_e32 v252, 0
	v_mov_b32_e32 v253, 0
	s_mov_b64 s[26:27], s[24:25]
	v_mov_b32_e32 v46, 0
	v_mov_b32_e32 v47, 0
	v_mov_b32_e32 v48, 0
	v_mov_b32_e32 v49, 0
	v_mov_b32_e32 v50, 0
	v_mov_b32_e32 v51, 0
	v_mov_b32_e32 v52, 0
	v_mov_b32_e32 v53, 0
	s_and_b32 s29, s46, 1
	s_cmp_eq_u32 s29, 0
	s_cselect_b32 s29, -1, 0
	s_cmp_lg_u32 s50, 0
	s_cselect_b32 s29, 1, s29
	s_add_i32 s49, s49, s29
	s_max_i32 s49, s49, 0
	s_min_i32 s49, s49, 60
	s_mov_b32 s50, 0
	s_mov_b32 s29, s49
	s_cmp_eq_u32 s49, 0
	s_cbranch_scc1 .Lrec_dle
.Lrec_dl:
	s_nop 7
	s_sub_u32 s29, s29, 1
	s_cmp_gt_i32 s29, 0
	s_cbranch_scc1 .Lrec_dl
.Lrec_dle:
	buffer_load_dwordx4 v[194:197], v242, s[20:23], 0 offen sc1
	buffer_load_dwordx4 v[198:201], v243, s[20:23], 0 offen sc1
	buffer_load_dwordx4 v[202:205], v244, s[20:23], 0 offen sc1
	buffer_load_dwordx4 v[206:209], v245, s[20:23], 0 offen sc1
	s_cmp_eq_u64 s[2:3], 0
	s_cbranch_scc1 .Lrec_noflush
	s_and_b32 s29, s46, 3
	s_cmp_lg_u32 s29, 0
	s_cbranch_scc1 .Lrec_noflush
	s_cmp_lt_u32 s46, 4
	s_cbranch_scc1 .Lrec_noflush
	s_add_i32 s29, s46, -4
	v_accvgpr_read_b32 v46, a94
	v_or_b32_e32 v50, s29, v46
	v_lshlrev_b32_e32 v46, 3, v50
	v_accvgpr_read_b32 v47, a95
	v_and_or_b32 v46, v46, 40, v47
	v_accvgpr_read_b32 v47, a96
	v_lshl_add_u32 v47, v47, 1, 0
	v_lshl_add_u32 v54, v46, 6, v47
	ds_read_b128 v[46:49], v54 offset:33024
	v_ashrrev_i32_e32 v51, 31, v50
	v_accvgpr_read_b32 v52, a100
	v_lshlrev_b64 v[50:51], 17, v[50:51]
	v_accvgpr_read_b32 v53, a101
	v_lshl_add_u64 v[50:51], v[52:53], 0, v[50:51]
	v_add_co_u32_e32 v52, vcc, 0x20000, v50
	s_nop 1
	v_addc_co_u32_e32 v53, vcc, 0, v51, vcc
	s_waitcnt lgkmcnt(0)
	global_store_dwordx4 v[52:53], v[46:49], off
	s_nop 1
	ds_read_b128 v[46:49], v54 offset:34048
	v_add_co_u32_e32 v50, vcc, 0x60000, v50
	s_nop 1
	v_addc_co_u32_e32 v51, vcc, 0, v51, vcc
	s_waitcnt lgkmcnt(0)
	global_store_dwordx4 v[50:51], v[46:49], off
	s_nop 1
	v_mov_b32_e32 v46, 0
	v_mov_b32_e32 v47, 0
	v_mov_b32_e32 v48, 0
	v_mov_b32_e32 v49, 0
	v_mov_b32_e32 v50, 0
	v_mov_b32_e32 v51, 0
	v_mov_b32_e32 v52, 0
	v_mov_b32_e32 v53, 0
